# P6 end-of-stage vmcnt waits count only the 4 prefetch loads (stores stay in flight)
# speedup vs baseline: 1.0019x; 1.0019x over previous
.LBB0_974:
	s_nop 0
	v_cndmask_b32_e64 v4, 0, 1, s[4:5]
	v_cmp_ne_u32_e64 s[38:39], 1, v4
	v_or_b32_e32 v4, s13, v180
	v_mad_u32_u24 v228, v4, s33, v2
	ds_read_b128 v[4:7], v228
	ds_read_b128 v[196:199], v228 offset:32
	ds_read_b128 v[204:207], v228 offset:64
	ds_read_b128 v[208:211], v228 offset:96
	ds_read_b128 v[212:215], v228 offset:128
	ds_read_b128 v[216:219], v228 offset:160
	ds_read_b128 v[220:223], v228 offset:192
	ds_read_b128 v[224:227], v228 offset:224
	s_waitcnt lgkmcnt(7)
	v_mfma_f32_32x32x16_bf16 v[20:35], v[36:39], v[4:7], 0
	v_mfma_f32_32x32x16_bf16 v[4:19], v[100:103], v[4:7], 0
	s_waitcnt lgkmcnt(6)
	v_mfma_f32_32x32x16_bf16 v[20:35], v[40:43], v[196:199], v[20:35]
	v_mfma_f32_32x32x16_bf16 v[4:19], v[104:107], v[196:199], v[4:19]
	s_waitcnt lgkmcnt(5)
	v_mfma_f32_32x32x16_bf16 v[20:35], v[44:47], v[204:207], v[20:35]
	v_mfma_f32_32x32x16_bf16 v[4:19], v[108:111], v[204:207], v[4:19]
	s_waitcnt lgkmcnt(4)
	v_mfma_f32_32x32x16_bf16 v[20:35], v[48:51], v[208:211], v[20:35]
	v_mfma_f32_32x32x16_bf16 v[4:19], v[112:115], v[208:211], v[4:19]
	s_waitcnt lgkmcnt(3)
	v_mfma_f32_32x32x16_bf16 v[20:35], v[52:55], v[212:215], v[20:35]
	v_mfma_f32_32x32x16_bf16 v[4:19], v[116:119], v[212:215], v[4:19]
	s_waitcnt lgkmcnt(2)
	v_mfma_f32_32x32x16_bf16 v[20:35], v[56:59], v[216:219], v[20:35]
	v_mfma_f32_32x32x16_bf16 v[4:19], v[120:123], v[216:219], v[4:19]
	s_waitcnt lgkmcnt(1)
	v_mfma_f32_32x32x16_bf16 v[20:35], v[60:63], v[220:223], v[20:35]
	v_mfma_f32_32x32x16_bf16 v[4:19], v[124:127], v[220:223], v[4:19]
	s_waitcnt lgkmcnt(0)
	v_mfma_f32_32x32x16_bf16 v[20:35], v[64:67], v[224:227], v[20:35]
	v_mfma_f32_32x32x16_bf16 v[4:19], v[128:131], v[224:227], v[4:19]
	ds_read_b128 v[196:199], v228 offset:256
	ds_read_b128 v[204:207], v228 offset:288
	ds_read_b128 v[208:211], v228 offset:320
	ds_read_b128 v[212:215], v228 offset:352
	ds_read_b128 v[216:219], v228 offset:384
	ds_read_b128 v[220:223], v228 offset:416
	ds_read_b128 v[224:227], v228 offset:448
	ds_read_b128 v[228:231], v228 offset:480
	s_waitcnt lgkmcnt(7)
	v_mfma_f32_32x32x16_bf16 v[20:35], v[68:71], v[196:199], v[20:35]
	s_mov_b64 s[4:5], 0
	v_mfma_f32_32x32x16_bf16 v[4:19], v[132:135], v[196:199], v[4:19]
	v_or_b32_e32 v196, s13, v194
	v_mov_b32_e32 v197, v195
	s_mov_b32 s13, 32
	s_waitcnt lgkmcnt(6)
	v_mfma_f32_32x32x16_bf16 v[20:35], v[72:75], v[204:207], v[20:35]
	v_mfma_f32_32x32x16_bf16 v[4:19], v[136:139], v[204:207], v[4:19]
	s_waitcnt lgkmcnt(5)
	v_mfma_f32_32x32x16_bf16 v[20:35], v[76:79], v[208:211], v[20:35]
	v_mfma_f32_32x32x16_bf16 v[4:19], v[140:143], v[208:211], v[4:19]
	s_waitcnt lgkmcnt(4)
	v_mfma_f32_32x32x16_bf16 v[20:35], v[80:83], v[212:215], v[20:35]
	v_mfma_f32_32x32x16_bf16 v[4:19], v[144:147], v[212:215], v[4:19]
	s_waitcnt lgkmcnt(3)
	v_mfma_f32_32x32x16_bf16 v[20:35], v[84:87], v[216:219], v[20:35]
	v_mfma_f32_32x32x16_bf16 v[4:19], v[148:151], v[216:219], v[4:19]
	s_waitcnt lgkmcnt(2)
	v_mfma_f32_32x32x16_bf16 v[20:35], v[88:91], v[220:223], v[20:35]
	v_mfma_f32_32x32x16_bf16 v[4:19], v[152:155], v[220:223], v[4:19]
	s_waitcnt lgkmcnt(1)
	v_mfma_f32_32x32x16_bf16 v[20:35], v[92:95], v[224:227], v[20:35]
	v_mfma_f32_32x32x16_bf16 v[4:19], v[160:163], v[224:227], v[4:19]
	s_waitcnt lgkmcnt(0)
	v_mfma_f32_32x32x16_bf16 v[20:35], v[96:99], v[228:231], v[20:35]
	v_mfma_f32_32x32x16_bf16 v[4:19], v[164:167], v[228:231], v[4:19]
	s_nop 10
	v_cvt_pk_bf16_f32 v20, v20, v21
	v_cvt_pk_bf16_f32 v21, v22, v23
	v_cvt_pk_bf16_f32 v22, v24, v25
	v_lshl_add_u64 v[24:25], v[196:197], 4, v[188:189]
	v_cvt_pk_bf16_f32 v23, v26, v27
	v_permlane32_swap_b32_e32 v20, v22
	v_cvt_pk_bf16_f32 v4, v4, v5
	v_cvt_pk_bf16_f32 v5, v6, v7
	v_cvt_pk_bf16_f32 v6, v8, v9
	v_cvt_pk_bf16_f32 v7, v10, v11
	v_add_co_u32_e32 v8, vcc, s25, v24
	v_permlane32_swap_b32_e32 v21, v23
	v_permlane32_swap_b32_e32 v4, v6
	v_permlane32_swap_b32_e32 v5, v7
	v_addc_co_u32_e32 v9, vcc, 0, v25, vcc
	global_store_dwordx4 v[24:25], v[20:23], off
	global_store_dwordx4 v[8:9], v[4:7], off
	s_and_b64 vcc, exec, s[38:39]
	v_cvt_pk_bf16_f32 v20, v28, v29
	v_cvt_pk_bf16_f32 v21, v30, v31
	v_cvt_pk_bf16_f32 v22, v32, v33
	v_cvt_pk_bf16_f32 v23, v34, v35
	v_cvt_pk_bf16_f32 v4, v12, v13
	v_cvt_pk_bf16_f32 v5, v14, v15
	v_cvt_pk_bf16_f32 v6, v16, v17
	v_cvt_pk_bf16_f32 v7, v18, v19
	v_permlane32_swap_b32_e32 v20, v22
	v_permlane32_swap_b32_e32 v21, v23
	v_permlane32_swap_b32_e32 v4, v6
	v_permlane32_swap_b32_e32 v5, v7
	global_store_dwordx4 v[24:25], v[20:23], off offset:2048
	global_store_dwordx4 v[8:9], v[4:7], off offset:2048
	s_cbranch_vccz .LBB0_974
	s_xor_b32 s9, s9, 1
	s_and_b64 vcc, exec, s[14:15]
	s_cbranch_vccz .LBB0_970
	s_mul_i32 s4, s9, 0x8400
	v_add_u32_e32 v2, s4, v181
	s_waitcnt vmcnt(11)
	ds_write_b128 v2, v[156:159]
	s_waitcnt vmcnt(10)
	ds_write_b128 v2, v[168:171] offset:8448
	s_waitcnt vmcnt(9)
	ds_write_b128 v2, v[172:175] offset:16896
	s_waitcnt vmcnt(8)
	ds_write_b128 v2, v[176:179] offset:25344
	s_branch .LBB0_970
